# SSD units: 64-lane prefix sum by six fused DPP adds (row_shr/row_bcast) instead of six ds_bpermute round trips
# baseline (speedup 1.0000x reference)
.LBB0_492:
	s_lshl_b32 s0, s26, 2
	s_or_b32 s9, s0, s34
	s_lshl_b32 s0, s25, 4
	s_lshl_b32 s1, s9, 1
	s_add_i32 s0, s0, s18
	s_add_i32 s8, s0, s1
	s_lshl_b32 s0, s9, 2
	v_mov_b32_e32 v2, s0
	global_load_dword v2, v2, s[62:63]
	s_mov_b32 s14, 0
	s_mov_b32 s15, 1
	s_mov_b32 s1, s14
	v_and_b32_e32 v7, 64, v203
	v_add_u32_e32 v8, -1, v203
	v_cmp_lt_i32_e32 vcc, v8, v7
	s_lshl_b32 s10, s9, 7
	s_mov_b32 s11, s14
	v_cndmask_b32_e32 v8, v8, v203, vcc
	v_lshlrev_b32_e32 v8, 2, v8
	s_waitcnt vmcnt(0)
	v_mul_f32_e32 v2, 0x3fb8aa3b, v2
	v_exp_f32_e32 v6, v2
	v_add_u32_e32 v2, s3, v76
	v_ashrrev_i32_e32 v3, 31, v2
	v_lshlrev_b64 v[4:5], 6, v[2:3]
	v_lshl_add_u64 v[4:5], s[64:65], 0, v[4:5]
	v_lshl_add_u64 v[4:5], v[4:5], 0, s[0:1]
	global_load_dword v4, v[4:5], off
	v_lshlrev_b64 v[2:3], 11, v[2:3]
	v_lshl_add_u64 v[2:3], s[60:61], 0, v[2:3]
	v_lshl_add_u64 v[14:15], v[2:3], 0, s[10:11]
	s_waitcnt vmcnt(0)
	v_mul_f32_e64 v5, v4, -v6
	s_nop 1
	v_add_f32_dpp v5, v5, v5 row_shr:1 row_mask:0xf bank_mask:0xf
	v_add_u32_e32 v8, -2, v203
	v_cmp_lt_i32_e32 vcc, v8, v7
	s_nop 1
	v_cndmask_b32_e32 v8, v8, v203, vcc
	v_lshlrev_b32_e32 v8, 2, v8
	s_nop 1
	v_add_f32_dpp v5, v5, v5 row_shr:2 row_mask:0xf bank_mask:0xf
	v_add_u32_e32 v8, -4, v203
	v_cmp_lt_i32_e32 vcc, v8, v7
	s_nop 1
	v_cndmask_b32_e32 v8, v8, v203, vcc
	v_lshlrev_b32_e32 v8, 2, v8
	s_nop 1
	v_add_f32_dpp v5, v5, v5 row_shr:4 row_mask:0xf bank_mask:0xf
	v_add_u32_e32 v8, -8, v203
	v_cmp_lt_i32_e32 vcc, v8, v7
	s_nop 1
	v_cndmask_b32_e32 v8, v8, v203, vcc
	v_lshlrev_b32_e32 v8, 2, v8
	s_nop 1
	v_add_f32_dpp v5, v5, v5 row_shr:8 row_mask:0xf bank_mask:0xf
	v_add_u32_e32 v8, -16, v203
	v_cmp_lt_i32_e32 vcc, v8, v7
	s_nop 1
	v_cndmask_b32_e32 v8, v8, v203, vcc
	v_lshlrev_b32_e32 v8, 2, v8
	s_nop 1
	v_add_f32_dpp v5, v5, v5 row_bcast:15 row_mask:0xa bank_mask:0xf
	v_subrev_u32_e32 v8, 32, v203
	v_cmp_lt_i32_e32 vcc, v8, v7
	s_nop 1
	v_cndmask_b32_e32 v7, v8, v203, vcc
	v_lshlrev_b32_e32 v7, 2, v7
	s_nop 1
	v_add_f32_dpp v5, v5, v5 row_bcast:31 row_mask:0xc bank_mask:0xf
	v_lshl_or_b32 v7, v203, 2, v251
	ds_bpermute_b32 v27, v7, v5
	s_waitcnt lgkmcnt(0)
	v_sub_f32_e32 v7, v27, v5
	v_fmac_f32_e32 v5, v4, v6
	v_cndmask_b32_e64 v5, v5, v7, s[38:39]
	v_mul_f32_e32 v5, 0x3fb8aa3b, v5
	v_exp_f32_e32 v5, v5
	s_nop 0
	v_mul_f32_e32 v29, v4, v5
	global_load_dwordx4 v[2:5], v[14:15], off offset:48
	global_load_dwordx4 v[6:9], v[14:15], off offset:32
	global_load_dwordx4 v[10:13], v[14:15], off offset:16
	global_load_dwordx4 v[68:71], v[14:15], off
	s_waitcnt vmcnt(0)
	v_lshlrev_b32_e32 v16, 16, v68
	v_mul_f32_e32 v16, v29, v16
	v_and_b32_e32 v17, 0xffff0000, v68
	v_cvt_pk_bf16_f32 v16, v16, s0
	ds_write_b16 v82, v16 offset:18432
	v_mul_f32_e32 v16, v29, v17
	v_lshlrev_b32_e32 v31, 16, v69
	v_cvt_pk_bf16_f32 v16, v16, s0
	ds_write_b16 v82, v16 offset:18576
	v_mul_f32_e32 v16, v29, v31
	v_and_b32_e32 v33, 0xffff0000, v69
	v_cvt_pk_bf16_f32 v16, v16, s0
	ds_write_b16 v82, v16 offset:18720
	v_mul_f32_e32 v16, v29, v33
	v_cvt_pk_bf16_f32 v16, v16, s0
	ds_write_b16 v82, v16 offset:18864
	v_lshlrev_b32_e32 v16, 16, v70
	v_mul_f32_e32 v16, v29, v16
	v_and_b32_e32 v17, 0xffff0000, v70
	v_cvt_pk_bf16_f32 v16, v16, s0
	ds_write_b16 v82, v16 offset:19008
	v_mul_f32_e32 v16, v29, v17
	v_lshlrev_b32_e32 v31, 16, v71
	v_cvt_pk_bf16_f32 v16, v16, s0
	ds_write_b16 v82, v16 offset:19152
	v_mul_f32_e32 v16, v29, v31
	v_and_b32_e32 v33, 0xffff0000, v71
	v_cvt_pk_bf16_f32 v16, v16, s0
	ds_write_b16 v82, v16 offset:19296
	v_mul_f32_e32 v16, v29, v33
	v_cvt_pk_bf16_f32 v16, v16, s0
	ds_write_b16 v82, v16 offset:19440
	v_lshlrev_b32_e32 v16, 16, v10
	v_and_b32_e32 v10, 0xffff0000, v10
	v_mul_f32_e32 v10, v29, v10
	v_lshlrev_b32_e32 v17, 16, v11
	v_cvt_pk_bf16_f32 v10, v10, s0
	ds_write_b16 v82, v10 offset:19728
	v_mul_f32_e32 v10, v29, v17
	v_and_b32_e32 v11, 0xffff0000, v11
	v_cvt_pk_bf16_f32 v10, v10, s0
	ds_write_b16 v82, v10 offset:19872
	v_mul_f32_e32 v10, v29, v11
	v_cvt_pk_bf16_f32 v10, v10, s0
	ds_write_b16 v82, v10 offset:20016
	v_lshlrev_b32_e32 v10, 16, v12
	v_mul_f32_e32 v10, v29, v10
	v_and_b32_e32 v11, 0xffff0000, v12
	v_cvt_pk_bf16_f32 v10, v10, s0
	ds_write_b16 v82, v10 offset:20160
	v_mul_f32_e32 v10, v29, v11
	v_lshlrev_b32_e32 v12, 16, v13
	v_cvt_pk_bf16_f32 v10, v10, s0
	ds_write_b16 v82, v10 offset:20304
	v_mul_f32_e32 v10, v29, v12
	v_and_b32_e32 v13, 0xffff0000, v13
	v_cvt_pk_bf16_f32 v10, v10, s0
	ds_write_b16 v82, v10 offset:20448
	v_mul_f32_e32 v10, v29, v13
	v_cvt_pk_bf16_f32 v10, v10, s0
	ds_write_b16 v82, v10 offset:20592
	v_lshlrev_b32_e32 v10, 16, v6
	v_and_b32_e32 v6, 0xffff0000, v6
	v_mul_f32_e32 v6, v29, v6
	v_lshlrev_b32_e32 v11, 16, v7
	v_cvt_pk_bf16_f32 v6, v6, s0
	ds_write_b16 v82, v6 offset:20880
	v_mul_f32_e32 v6, v29, v11
	v_and_b32_e32 v7, 0xffff0000, v7
	v_cvt_pk_bf16_f32 v6, v6, s0
	ds_write_b16 v82, v6 offset:21024
	v_mul_f32_e32 v6, v29, v7
	v_cvt_pk_bf16_f32 v6, v6, s0
	ds_write_b16 v82, v6 offset:21168
	v_lshlrev_b32_e32 v6, 16, v8
	v_mul_f32_e32 v6, v29, v6
	v_and_b32_e32 v7, 0xffff0000, v8
	v_cvt_pk_bf16_f32 v6, v6, s0
	ds_write_b16 v82, v6 offset:21312
	v_mul_f32_e32 v6, v29, v7
	v_lshlrev_b32_e32 v8, 16, v9
	v_cvt_pk_bf16_f32 v6, v6, s0
	ds_write_b16 v82, v6 offset:21456
	v_mul_f32_e32 v6, v29, v8
	v_and_b32_e32 v9, 0xffff0000, v9
	v_cvt_pk_bf16_f32 v6, v6, s0
	ds_write_b16 v82, v6 offset:21600
	v_mul_f32_e32 v6, v29, v9
	v_cvt_pk_bf16_f32 v6, v6, s0
	ds_write_b16 v82, v6 offset:21744
	v_lshlrev_b32_e32 v6, 16, v2
	v_and_b32_e32 v2, 0xffff0000, v2
	v_mul_f32_e32 v2, v29, v2
	v_lshlrev_b32_e32 v7, 16, v3
	v_cvt_pk_bf16_f32 v2, v2, s0
	ds_write_b16 v82, v2 offset:22032
	v_mul_f32_e32 v2, v29, v7
	v_and_b32_e32 v3, 0xffff0000, v3
	v_cvt_pk_bf16_f32 v2, v2, s0
	ds_write_b16 v82, v2 offset:22176
	v_mul_f32_e32 v2, v29, v3
	v_cvt_pk_bf16_f32 v2, v2, s0
	ds_write_b16 v82, v2 offset:22320
	v_lshlrev_b32_e32 v2, 16, v4
	v_mul_f32_e32 v2, v29, v2
	v_and_b32_e32 v3, 0xffff0000, v4
	v_cvt_pk_bf16_f32 v2, v2, s0
	ds_write_b16 v82, v2 offset:22464
	v_mul_f32_e32 v2, v29, v3
	v_lshlrev_b32_e32 v4, 16, v5
	v_cvt_pk_bf16_f32 v2, v2, s0
	ds_write_b16 v82, v2 offset:22608
	v_mul_f32_e32 v2, v29, v4
	v_and_b32_e32 v5, 0xffff0000, v5
	v_cvt_pk_bf16_f32 v2, v2, s0
	v_mul_f32_e32 v16, v29, v16
	v_mul_f32_e32 v10, v29, v10
	v_mul_f32_e32 v6, v29, v6
	ds_write_b16 v82, v2 offset:22752
	v_mul_f32_e32 v2, v29, v5
	v_cvt_pk_bf16_f32 v16, v16, s0
	v_cvt_pk_bf16_f32 v10, v10, s0
	v_cvt_pk_bf16_f32 v6, v6, s0
	v_cvt_pk_bf16_f32 v2, v2, s0
	ds_write_b16 v82, v16 offset:19584
	ds_write_b16 v82, v10 offset:20736
	ds_write_b16 v82, v6 offset:21888
	ds_write_b16 v82, v2 offset:22896
	global_load_dwordx4 v[2:5], v[14:15], off offset:112
	global_load_dwordx4 v[6:9], v[14:15], off offset:96
	global_load_dwordx4 v[10:13], v[14:15], off offset:80
	s_nop 0
	global_load_dwordx4 v[14:17], v[14:15], off offset:64
	s_waitcnt vmcnt(0)
	v_lshlrev_b32_e32 v31, 16, v14
	v_and_b32_e32 v14, 0xffff0000, v14
	v_mul_f32_e32 v14, v29, v14
	v_lshlrev_b32_e32 v33, 16, v15
	v_cvt_pk_bf16_f32 v14, v14, s0
	ds_write_b16 v82, v14 offset:23184
	v_mul_f32_e32 v14, v29, v33
	v_and_b32_e32 v15, 0xffff0000, v15
	v_cvt_pk_bf16_f32 v14, v14, s0
	ds_write_b16 v82, v14 offset:23328
	v_mul_f32_e32 v14, v29, v15
	v_cvt_pk_bf16_f32 v14, v14, s0
	ds_write_b16 v82, v14 offset:23472
	v_lshlrev_b32_e32 v14, 16, v16
	v_mul_f32_e32 v14, v29, v14
	v_and_b32_e32 v15, 0xffff0000, v16
	v_cvt_pk_bf16_f32 v14, v14, s0
	ds_write_b16 v82, v14 offset:23616
	v_mul_f32_e32 v14, v29, v15
	v_lshlrev_b32_e32 v16, 16, v17
	v_cvt_pk_bf16_f32 v14, v14, s0
	ds_write_b16 v82, v14 offset:23760
	v_mul_f32_e32 v14, v29, v16
	v_and_b32_e32 v17, 0xffff0000, v17
	v_cvt_pk_bf16_f32 v14, v14, s0
	ds_write_b16 v82, v14 offset:23904
	v_mul_f32_e32 v14, v29, v17
	v_cvt_pk_bf16_f32 v14, v14, s0
	ds_write_b16 v82, v14 offset:24048
	v_lshlrev_b32_e32 v14, 16, v10
	v_and_b32_e32 v10, 0xffff0000, v10
	v_mul_f32_e32 v10, v29, v10
	v_lshlrev_b32_e32 v15, 16, v11
	v_cvt_pk_bf16_f32 v10, v10, s0
	ds_write_b16 v82, v10 offset:24336
	v_mul_f32_e32 v10, v29, v15
	v_and_b32_e32 v11, 0xffff0000, v11
	v_cvt_pk_bf16_f32 v10, v10, s0
	ds_write_b16 v82, v10 offset:24480
	v_mul_f32_e32 v10, v29, v11
	v_cvt_pk_bf16_f32 v10, v10, s0
	ds_write_b16 v82, v10 offset:24624
	v_lshlrev_b32_e32 v10, 16, v12
	v_mul_f32_e32 v10, v29, v10
	v_and_b32_e32 v11, 0xffff0000, v12
	v_cvt_pk_bf16_f32 v10, v10, s0
	ds_write_b16 v82, v10 offset:24768
	v_mul_f32_e32 v10, v29, v11
	v_lshlrev_b32_e32 v12, 16, v13
	v_cvt_pk_bf16_f32 v10, v10, s0
	ds_write_b16 v82, v10 offset:24912
	v_mul_f32_e32 v10, v29, v12
	v_and_b32_e32 v13, 0xffff0000, v13
	v_cvt_pk_bf16_f32 v10, v10, s0
	ds_write_b16 v82, v10 offset:25056
	v_mul_f32_e32 v10, v29, v13
	v_cvt_pk_bf16_f32 v10, v10, s0
	ds_write_b16 v82, v10 offset:25200
	v_lshlrev_b32_e32 v10, 16, v6
	v_and_b32_e32 v6, 0xffff0000, v6
	v_mul_f32_e32 v6, v29, v6
	v_lshlrev_b32_e32 v11, 16, v7
	v_cvt_pk_bf16_f32 v6, v6, s0
	ds_write_b16 v82, v6 offset:25488
	v_mul_f32_e32 v6, v29, v11
	v_and_b32_e32 v7, 0xffff0000, v7
	v_cvt_pk_bf16_f32 v6, v6, s0
	ds_write_b16 v82, v6 offset:25632
	v_mul_f32_e32 v6, v29, v7
	v_cvt_pk_bf16_f32 v6, v6, s0
	ds_write_b16 v82, v6 offset:25776
	v_lshlrev_b32_e32 v6, 16, v8
	v_mul_f32_e32 v6, v29, v6
	v_and_b32_e32 v7, 0xffff0000, v8
	v_cvt_pk_bf16_f32 v6, v6, s0
	ds_write_b16 v82, v6 offset:25920
	v_mul_f32_e32 v6, v29, v7
	v_lshlrev_b32_e32 v8, 16, v9
	v_cvt_pk_bf16_f32 v6, v6, s0
	ds_write_b16 v82, v6 offset:26064
	v_mul_f32_e32 v6, v29, v8
	v_and_b32_e32 v9, 0xffff0000, v9
	v_cvt_pk_bf16_f32 v6, v6, s0
	ds_write_b16 v82, v6 offset:26208
	v_mul_f32_e32 v6, v29, v9
	v_cvt_pk_bf16_f32 v6, v6, s0
	ds_write_b16 v82, v6 offset:26352
	v_lshlrev_b32_e32 v6, 16, v2
	v_and_b32_e32 v2, 0xffff0000, v2
	v_mul_f32_e32 v2, v29, v2
	v_lshlrev_b32_e32 v7, 16, v3
	v_cvt_pk_bf16_f32 v2, v2, s0
	ds_write_b16 v82, v2 offset:26640
	v_mul_f32_e32 v2, v29, v7
	v_and_b32_e32 v3, 0xffff0000, v3
	v_cvt_pk_bf16_f32 v2, v2, s0
	ds_write_b16 v82, v2 offset:26784
	v_mul_f32_e32 v2, v29, v3
	v_cvt_pk_bf16_f32 v2, v2, s0
	ds_write_b16 v82, v2 offset:26928
	v_lshlrev_b32_e32 v2, 16, v4
	v_mul_f32_e32 v2, v29, v2
	v_and_b32_e32 v3, 0xffff0000, v4
	v_cvt_pk_bf16_f32 v2, v2, s0
	ds_write_b16 v82, v2 offset:27072
	v_mul_f32_e32 v2, v29, v3
	v_lshlrev_b32_e32 v4, 16, v5
	v_cvt_pk_bf16_f32 v2, v2, s0
	ds_write_b16 v82, v2 offset:27216
	v_mul_f32_e32 v2, v29, v4
	v_and_b32_e32 v5, 0xffff0000, v5
	v_cvt_pk_bf16_f32 v2, v2, s0
	v_mul_f32_e32 v31, v29, v31
	v_mul_f32_e32 v14, v29, v14
	v_mul_f32_e32 v10, v29, v10
	v_mul_f32_e32 v6, v29, v6
	ds_write_b16 v82, v2 offset:27360
	v_mul_f32_e32 v2, v29, v5
	v_cvt_pk_bf16_f32 v31, v31, s0
	v_cvt_pk_bf16_f32 v14, v14, s0
	v_cvt_pk_bf16_f32 v10, v10, s0
	v_cvt_pk_bf16_f32 v6, v6, s0
	v_cvt_pk_bf16_f32 v2, v2, s0
	ds_write_b16 v82, v31 offset:23040
	ds_write_b16 v82, v14 offset:24192
	ds_write_b16 v82, v10 offset:25344
	ds_write_b16 v82, v6 offset:26496
	ds_write_b16 v82, v2 offset:27504
	s_and_saveexec_b64 s[0:1], s[48:49]
	s_xor_b64 s[0:1], exec, s[0:1]
	s_ashr_i32 s9, s8, 31
	s_ashr_i32 s3, s2, 31
	s_or_saveexec_b64 s[0:1], s[0:1]
	v_mov_b64_e32 v[4:5], s[2:3]
	v_mov_b64_e32 v[2:3], s[8:9]
	s_xor_b64 exec, exec, s[0:1]
	s_cbranch_execz .LBB0_496
	v_mul_f32_e32 v2, 0x3fb8aa3b, v27
	s_ashr_i32 s9, s8, 31
	s_ashr_i32 s3, s2, 31
	s_mul_i32 s11, s8, 0x110
	v_exp_f32_e32 v2, v2
	s_mul_hi_i32 s10, s8, 0x110
	s_add_u32 s14, s22, s11
	s_addc_u32 s15, s23, s10
	s_lshl_b64 s[10:11], s[2:3], 2
	s_add_u32 s10, s14, s10
	s_addc_u32 s11, s15, s11
	global_store_dword v35, v2, s[10:11] nt
	v_mov_b64_e32 v[4:5], s[2:3]
	v_mov_b64_e32 v[2:3], s[8:9]

.LBB0_757:
	s_lshl_b32 s0, s27, 2
	s_or_b32 s9, s0, s18
	s_lshl_b32 s0, s26, 4
	s_lshl_b32 s1, s9, 1
	s_add_i32 s0, s0, s19
	s_add_i32 s8, s0, s1
	s_lshl_b32 s0, s9, 2
	v_mov_b32_e32 v2, s0
	global_load_dword v2, v2, s[66:67]
	s_mov_b32 s14, 0
	s_mov_b32 s15, 1
	s_mov_b32 s1, s14
	v_and_b32_e32 v7, 64, v203
	v_add_u32_e32 v8, -1, v203
	v_cmp_lt_i32_e32 vcc, v8, v7
	s_lshl_b32 s10, s9, 7
	s_mov_b32 s11, s14
	v_cndmask_b32_e32 v8, v8, v203, vcc
	v_lshlrev_b32_e32 v8, 2, v8
	s_waitcnt vmcnt(0)
	v_mul_f32_e32 v2, 0x3fb8aa3b, v2
	v_exp_f32_e32 v6, v2
	v_add_u32_e32 v2, s3, v140
	v_ashrrev_i32_e32 v3, 31, v2
	v_lshlrev_b64 v[4:5], 6, v[2:3]
	v_lshl_add_u64 v[4:5], s[68:69], 0, v[4:5]
	v_lshl_add_u64 v[4:5], v[4:5], 0, s[0:1]
	global_load_dword v4, v[4:5], off
	v_lshlrev_b64 v[2:3], 11, v[2:3]
	v_lshl_add_u64 v[2:3], s[64:65], 0, v[2:3]
	v_lshl_add_u64 v[14:15], v[2:3], 0, s[10:11]
	s_waitcnt vmcnt(0)
	v_mul_f32_e64 v5, v4, -v6
	s_nop 1
	v_add_f32_dpp v5, v5, v5 row_shr:1 row_mask:0xf bank_mask:0xf
	v_add_u32_e32 v8, -2, v203
	v_cmp_lt_i32_e32 vcc, v8, v7
	s_nop 1
	v_cndmask_b32_e32 v8, v8, v203, vcc
	v_lshlrev_b32_e32 v8, 2, v8
	s_nop 1
	v_add_f32_dpp v5, v5, v5 row_shr:2 row_mask:0xf bank_mask:0xf
	v_add_u32_e32 v8, -4, v203
	v_cmp_lt_i32_e32 vcc, v8, v7
	s_nop 1
	v_cndmask_b32_e32 v8, v8, v203, vcc
	v_lshlrev_b32_e32 v8, 2, v8
	s_nop 1
	v_add_f32_dpp v5, v5, v5 row_shr:4 row_mask:0xf bank_mask:0xf
	v_add_u32_e32 v8, -8, v203
	v_cmp_lt_i32_e32 vcc, v8, v7
	s_nop 1
	v_cndmask_b32_e32 v8, v8, v203, vcc
	v_lshlrev_b32_e32 v8, 2, v8
	s_nop 1
	v_add_f32_dpp v5, v5, v5 row_shr:8 row_mask:0xf bank_mask:0xf
	v_add_u32_e32 v8, -16, v203
	v_cmp_lt_i32_e32 vcc, v8, v7
	s_nop 1
	v_cndmask_b32_e32 v8, v8, v203, vcc
	v_lshlrev_b32_e32 v8, 2, v8
	s_nop 1
	v_add_f32_dpp v5, v5, v5 row_bcast:15 row_mask:0xa bank_mask:0xf
	v_subrev_u32_e32 v8, 32, v203
	v_cmp_lt_i32_e32 vcc, v8, v7
	s_nop 1
	v_cndmask_b32_e32 v7, v8, v203, vcc
	v_lshlrev_b32_e32 v7, 2, v7
	s_nop 1
	v_add_f32_dpp v5, v5, v5 row_bcast:31 row_mask:0xc bank_mask:0xf
	v_lshl_or_b32 v7, v203, 2, v251
	ds_bpermute_b32 v27, v7, v5
	s_waitcnt lgkmcnt(0)
	v_sub_f32_e32 v7, v27, v5
	v_fmac_f32_e32 v5, v4, v6
	v_cndmask_b32_e64 v5, v5, v7, s[28:29]
	v_mul_f32_e32 v5, 0x3fb8aa3b, v5
	v_exp_f32_e32 v5, v5
	s_nop 0
	v_mul_f32_e32 v29, v4, v5
	global_load_dwordx4 v[2:5], v[14:15], off offset:48
	global_load_dwordx4 v[6:9], v[14:15], off offset:32
	global_load_dwordx4 v[10:13], v[14:15], off offset:16
	global_load_dwordx4 v[68:71], v[14:15], off
	s_waitcnt vmcnt(0)
	v_lshlrev_b32_e32 v16, 16, v68
	v_mul_f32_e32 v16, v29, v16
	v_and_b32_e32 v17, 0xffff0000, v68
	v_cvt_pk_bf16_f32 v16, v16, s0
	ds_write_b16 v80, v16 offset:18432
	v_mul_f32_e32 v16, v29, v17
	v_lshlrev_b32_e32 v31, 16, v69
	v_cvt_pk_bf16_f32 v16, v16, s0
	ds_write_b16 v80, v16 offset:18576
	v_mul_f32_e32 v16, v29, v31
	v_and_b32_e32 v33, 0xffff0000, v69
	v_cvt_pk_bf16_f32 v16, v16, s0
	ds_write_b16 v80, v16 offset:18720
	v_mul_f32_e32 v16, v29, v33
	v_cvt_pk_bf16_f32 v16, v16, s0
	ds_write_b16 v80, v16 offset:18864
	v_lshlrev_b32_e32 v16, 16, v70
	v_mul_f32_e32 v16, v29, v16
	v_and_b32_e32 v17, 0xffff0000, v70
	v_cvt_pk_bf16_f32 v16, v16, s0
	ds_write_b16 v80, v16 offset:19008
	v_mul_f32_e32 v16, v29, v17
	v_lshlrev_b32_e32 v31, 16, v71
	v_cvt_pk_bf16_f32 v16, v16, s0
	ds_write_b16 v80, v16 offset:19152
	v_mul_f32_e32 v16, v29, v31
	v_and_b32_e32 v33, 0xffff0000, v71
	v_cvt_pk_bf16_f32 v16, v16, s0
	ds_write_b16 v80, v16 offset:19296
	v_mul_f32_e32 v16, v29, v33
	v_cvt_pk_bf16_f32 v16, v16, s0
	ds_write_b16 v80, v16 offset:19440
	v_lshlrev_b32_e32 v16, 16, v10
	v_and_b32_e32 v10, 0xffff0000, v10
	v_mul_f32_e32 v10, v29, v10
	v_lshlrev_b32_e32 v17, 16, v11
	v_cvt_pk_bf16_f32 v10, v10, s0
	ds_write_b16 v80, v10 offset:19728
	v_mul_f32_e32 v10, v29, v17
	v_and_b32_e32 v11, 0xffff0000, v11
	v_cvt_pk_bf16_f32 v10, v10, s0
	ds_write_b16 v80, v10 offset:19872
	v_mul_f32_e32 v10, v29, v11
	v_cvt_pk_bf16_f32 v10, v10, s0
	ds_write_b16 v80, v10 offset:20016
	v_lshlrev_b32_e32 v10, 16, v12
	v_mul_f32_e32 v10, v29, v10
	v_and_b32_e32 v11, 0xffff0000, v12
	v_cvt_pk_bf16_f32 v10, v10, s0
	ds_write_b16 v80, v10 offset:20160
	v_mul_f32_e32 v10, v29, v11
	v_lshlrev_b32_e32 v12, 16, v13
	v_cvt_pk_bf16_f32 v10, v10, s0
	ds_write_b16 v80, v10 offset:20304
	v_mul_f32_e32 v10, v29, v12
	v_and_b32_e32 v13, 0xffff0000, v13
	v_cvt_pk_bf16_f32 v10, v10, s0
	ds_write_b16 v80, v10 offset:20448
	v_mul_f32_e32 v10, v29, v13
	v_cvt_pk_bf16_f32 v10, v10, s0
	ds_write_b16 v80, v10 offset:20592
	v_lshlrev_b32_e32 v10, 16, v6
	v_and_b32_e32 v6, 0xffff0000, v6
	v_mul_f32_e32 v6, v29, v6
	v_lshlrev_b32_e32 v11, 16, v7
	v_cvt_pk_bf16_f32 v6, v6, s0
	ds_write_b16 v80, v6 offset:20880
	v_mul_f32_e32 v6, v29, v11
	v_and_b32_e32 v7, 0xffff0000, v7
	v_cvt_pk_bf16_f32 v6, v6, s0
	ds_write_b16 v80, v6 offset:21024
	v_mul_f32_e32 v6, v29, v7
	v_cvt_pk_bf16_f32 v6, v6, s0
	ds_write_b16 v80, v6 offset:21168
	v_lshlrev_b32_e32 v6, 16, v8
	v_mul_f32_e32 v6, v29, v6
	v_and_b32_e32 v7, 0xffff0000, v8
	v_cvt_pk_bf16_f32 v6, v6, s0
	ds_write_b16 v80, v6 offset:21312
	v_mul_f32_e32 v6, v29, v7
	v_lshlrev_b32_e32 v8, 16, v9
	v_cvt_pk_bf16_f32 v6, v6, s0
	ds_write_b16 v80, v6 offset:21456
	v_mul_f32_e32 v6, v29, v8
	v_and_b32_e32 v9, 0xffff0000, v9
	v_cvt_pk_bf16_f32 v6, v6, s0
	ds_write_b16 v80, v6 offset:21600
	v_mul_f32_e32 v6, v29, v9
	v_cvt_pk_bf16_f32 v6, v6, s0
	ds_write_b16 v80, v6 offset:21744
	v_lshlrev_b32_e32 v6, 16, v2
	v_and_b32_e32 v2, 0xffff0000, v2
	v_mul_f32_e32 v2, v29, v2
	v_lshlrev_b32_e32 v7, 16, v3
	v_cvt_pk_bf16_f32 v2, v2, s0
	ds_write_b16 v80, v2 offset:22032
	v_mul_f32_e32 v2, v29, v7
	v_and_b32_e32 v3, 0xffff0000, v3
	v_cvt_pk_bf16_f32 v2, v2, s0
	ds_write_b16 v80, v2 offset:22176
	v_mul_f32_e32 v2, v29, v3
	v_cvt_pk_bf16_f32 v2, v2, s0
	ds_write_b16 v80, v2 offset:22320
	v_lshlrev_b32_e32 v2, 16, v4
	v_mul_f32_e32 v2, v29, v2
	v_and_b32_e32 v3, 0xffff0000, v4
	v_cvt_pk_bf16_f32 v2, v2, s0
	ds_write_b16 v80, v2 offset:22464
	v_mul_f32_e32 v2, v29, v3
	v_lshlrev_b32_e32 v4, 16, v5
	v_cvt_pk_bf16_f32 v2, v2, s0
	ds_write_b16 v80, v2 offset:22608
	v_mul_f32_e32 v2, v29, v4
	v_and_b32_e32 v5, 0xffff0000, v5
	v_cvt_pk_bf16_f32 v2, v2, s0
	v_mul_f32_e32 v16, v29, v16
	v_mul_f32_e32 v10, v29, v10
	v_mul_f32_e32 v6, v29, v6
	ds_write_b16 v80, v2 offset:22752
	v_mul_f32_e32 v2, v29, v5
	v_cvt_pk_bf16_f32 v16, v16, s0
	v_cvt_pk_bf16_f32 v10, v10, s0
	v_cvt_pk_bf16_f32 v6, v6, s0
	v_cvt_pk_bf16_f32 v2, v2, s0
	ds_write_b16 v80, v16 offset:19584
	ds_write_b16 v80, v10 offset:20736
	ds_write_b16 v80, v6 offset:21888
	ds_write_b16 v80, v2 offset:22896
	global_load_dwordx4 v[2:5], v[14:15], off offset:112
	global_load_dwordx4 v[6:9], v[14:15], off offset:96
	global_load_dwordx4 v[10:13], v[14:15], off offset:80
	s_nop 0
	global_load_dwordx4 v[14:17], v[14:15], off offset:64
	s_waitcnt vmcnt(0)
	v_lshlrev_b32_e32 v31, 16, v14
	v_and_b32_e32 v14, 0xffff0000, v14
	v_mul_f32_e32 v14, v29, v14
	v_lshlrev_b32_e32 v33, 16, v15
	v_cvt_pk_bf16_f32 v14, v14, s0
	ds_write_b16 v80, v14 offset:23184
	v_mul_f32_e32 v14, v29, v33
	v_and_b32_e32 v15, 0xffff0000, v15
	v_cvt_pk_bf16_f32 v14, v14, s0
	ds_write_b16 v80, v14 offset:23328
	v_mul_f32_e32 v14, v29, v15
	v_cvt_pk_bf16_f32 v14, v14, s0
	ds_write_b16 v80, v14 offset:23472
	v_lshlrev_b32_e32 v14, 16, v16
	v_mul_f32_e32 v14, v29, v14
	v_and_b32_e32 v15, 0xffff0000, v16
	v_cvt_pk_bf16_f32 v14, v14, s0
	ds_write_b16 v80, v14 offset:23616
	v_mul_f32_e32 v14, v29, v15
	v_lshlrev_b32_e32 v16, 16, v17
	v_cvt_pk_bf16_f32 v14, v14, s0
	ds_write_b16 v80, v14 offset:23760
	v_mul_f32_e32 v14, v29, v16
	v_and_b32_e32 v17, 0xffff0000, v17
	v_cvt_pk_bf16_f32 v14, v14, s0
	ds_write_b16 v80, v14 offset:23904
	v_mul_f32_e32 v14, v29, v17
	v_cvt_pk_bf16_f32 v14, v14, s0
	ds_write_b16 v80, v14 offset:24048
	v_lshlrev_b32_e32 v14, 16, v10
	v_and_b32_e32 v10, 0xffff0000, v10
	v_mul_f32_e32 v10, v29, v10
	v_lshlrev_b32_e32 v15, 16, v11
	v_cvt_pk_bf16_f32 v10, v10, s0
	ds_write_b16 v80, v10 offset:24336
	v_mul_f32_e32 v10, v29, v15
	v_and_b32_e32 v11, 0xffff0000, v11
	v_cvt_pk_bf16_f32 v10, v10, s0
	ds_write_b16 v80, v10 offset:24480
	v_mul_f32_e32 v10, v29, v11
	v_cvt_pk_bf16_f32 v10, v10, s0
	ds_write_b16 v80, v10 offset:24624
	v_lshlrev_b32_e32 v10, 16, v12
	v_mul_f32_e32 v10, v29, v10
	v_and_b32_e32 v11, 0xffff0000, v12
	v_cvt_pk_bf16_f32 v10, v10, s0
	ds_write_b16 v80, v10 offset:24768
	v_mul_f32_e32 v10, v29, v11
	v_lshlrev_b32_e32 v12, 16, v13
	v_cvt_pk_bf16_f32 v10, v10, s0
	ds_write_b16 v80, v10 offset:24912
	v_mul_f32_e32 v10, v29, v12
	v_and_b32_e32 v13, 0xffff0000, v13
	v_cvt_pk_bf16_f32 v10, v10, s0
	ds_write_b16 v80, v10 offset:25056
	v_mul_f32_e32 v10, v29, v13
	v_cvt_pk_bf16_f32 v10, v10, s0
	ds_write_b16 v80, v10 offset:25200
	v_lshlrev_b32_e32 v10, 16, v6
	v_and_b32_e32 v6, 0xffff0000, v6
	v_mul_f32_e32 v6, v29, v6
	v_lshlrev_b32_e32 v11, 16, v7
	v_cvt_pk_bf16_f32 v6, v6, s0
	ds_write_b16 v80, v6 offset:25488
	v_mul_f32_e32 v6, v29, v11
	v_and_b32_e32 v7, 0xffff0000, v7
	v_cvt_pk_bf16_f32 v6, v6, s0
	ds_write_b16 v80, v6 offset:25632
	v_mul_f32_e32 v6, v29, v7
	v_cvt_pk_bf16_f32 v6, v6, s0
	ds_write_b16 v80, v6 offset:25776
	v_lshlrev_b32_e32 v6, 16, v8
	v_mul_f32_e32 v6, v29, v6
	v_and_b32_e32 v7, 0xffff0000, v8
	v_cvt_pk_bf16_f32 v6, v6, s0
	ds_write_b16 v80, v6 offset:25920
	v_mul_f32_e32 v6, v29, v7
	v_lshlrev_b32_e32 v8, 16, v9
	v_cvt_pk_bf16_f32 v6, v6, s0
	ds_write_b16 v80, v6 offset:26064
	v_mul_f32_e32 v6, v29, v8
	v_and_b32_e32 v9, 0xffff0000, v9
	v_cvt_pk_bf16_f32 v6, v6, s0
	ds_write_b16 v80, v6 offset:26208
	v_mul_f32_e32 v6, v29, v9
	v_cvt_pk_bf16_f32 v6, v6, s0
	ds_write_b16 v80, v6 offset:26352
	v_lshlrev_b32_e32 v6, 16, v2
	v_and_b32_e32 v2, 0xffff0000, v2
	v_mul_f32_e32 v2, v29, v2
	v_lshlrev_b32_e32 v7, 16, v3
	v_cvt_pk_bf16_f32 v2, v2, s0
	ds_write_b16 v80, v2 offset:26640
	v_mul_f32_e32 v2, v29, v7
	v_and_b32_e32 v3, 0xffff0000, v3
	v_cvt_pk_bf16_f32 v2, v2, s0
	ds_write_b16 v80, v2 offset:26784
	v_mul_f32_e32 v2, v29, v3
	v_cvt_pk_bf16_f32 v2, v2, s0
	ds_write_b16 v80, v2 offset:26928
	v_lshlrev_b32_e32 v2, 16, v4
	v_mul_f32_e32 v2, v29, v2
	v_and_b32_e32 v3, 0xffff0000, v4
	v_cvt_pk_bf16_f32 v2, v2, s0
	ds_write_b16 v80, v2 offset:27072
	v_mul_f32_e32 v2, v29, v3
	v_lshlrev_b32_e32 v4, 16, v5
	v_cvt_pk_bf16_f32 v2, v2, s0
	ds_write_b16 v80, v2 offset:27216
	v_mul_f32_e32 v2, v29, v4
	v_and_b32_e32 v5, 0xffff0000, v5
	v_cvt_pk_bf16_f32 v2, v2, s0
	v_mul_f32_e32 v31, v29, v31
	v_mul_f32_e32 v14, v29, v14
	v_mul_f32_e32 v10, v29, v10
	v_mul_f32_e32 v6, v29, v6
	ds_write_b16 v80, v2 offset:27360
	v_mul_f32_e32 v2, v29, v5
	v_cvt_pk_bf16_f32 v31, v31, s0
	v_cvt_pk_bf16_f32 v14, v14, s0
	v_cvt_pk_bf16_f32 v10, v10, s0
	v_cvt_pk_bf16_f32 v6, v6, s0
	v_cvt_pk_bf16_f32 v2, v2, s0
	ds_write_b16 v80, v31 offset:23040
	ds_write_b16 v80, v14 offset:24192
	ds_write_b16 v80, v10 offset:25344
	ds_write_b16 v80, v6 offset:26496
	ds_write_b16 v80, v2 offset:27504
	s_and_saveexec_b64 s[0:1], s[48:49]
	s_xor_b64 s[0:1], exec, s[0:1]
	s_ashr_i32 s9, s8, 31
	s_ashr_i32 s3, s2, 31
	s_or_saveexec_b64 s[0:1], s[0:1]
	v_mov_b64_e32 v[4:5], s[2:3]
	v_mov_b64_e32 v[2:3], s[8:9]
	s_xor_b64 exec, exec, s[0:1]
	s_cbranch_execz .LBB0_761
	v_mul_f32_e32 v2, 0x3fb8aa3b, v27
	s_ashr_i32 s9, s8, 31
	s_ashr_i32 s3, s2, 31
	s_mul_i32 s11, s8, 0x110
	v_exp_f32_e32 v2, v2
	s_mul_hi_i32 s10, s8, 0x110
	s_add_u32 s14, s23, s11
	s_addc_u32 s15, s24, s10
	s_lshl_b64 s[10:11], s[2:3], 2
	s_add_u32 s10, s14, s10
	s_addc_u32 s11, s15, s11
	global_store_dword v35, v2, s[10:11]
	v_mov_b64_e32 v[4:5], s[2:3]
	v_mov_b64_e32 v[2:3], s[8:9]

.LBB0_1026:
	s_lshl_b32 s0, s27, 2
	s_or_b32 s0, s0, s22
	s_lshl_b32 s1, s26, 4
	s_lshl_b32 s8, s0, 1
	s_add_i32 s1, s1, s23
	s_add_i32 s1, s1, s8
	s_mul_hi_i32 s9, s1, 0x44
	s_mulk_i32 s1, 0x44
	s_ashr_i32 s10, s3, 31
	s_add_u32 s8, s1, s3
	s_addc_u32 s9, s9, s10
	s_lshl_b64 s[8:9], s[8:9], 14
	v_lshl_add_u64 v[52:53], v[150:151], 0, s[8:9]
	s_movk_i32 s1, 0x1000
	v_add_co_u32_e32 v30, vcc, s1, v52
	s_movk_i32 s1, 0x3000
	s_nop 0
	v_addc_co_u32_e32 v31, vcc, 0, v53, vcc
	v_add_co_u32_e32 v48, vcc, s92, v52
	s_lshl_b32 s8, s0, 2
	s_nop 0
	v_addc_co_u32_e32 v49, vcc, 0, v53, vcc
	v_add_co_u32_e32 v64, vcc, s1, v52
	v_mov_b32_e32 v34, s8
	s_nop 0
	v_addc_co_u32_e32 v65, vcc, 0, v53, vcc
	global_load_dwordx4 v[2:5], v[52:53], off
	global_load_dwordx4 v[6:9], v[52:53], off offset:64
	global_load_dwordx4 v[10:13], v[52:53], off offset:128
	global_load_dwordx4 v[14:17], v[52:53], off offset:192
	global_load_dwordx4 v[18:21], v[48:49], off offset:-4096
	global_load_dwordx4 v[22:25], v[30:31], off offset:64
	global_load_dwordx4 v[26:29], v[30:31], off offset:128
	s_nop 0
	global_load_dwordx4 v[30:33], v[30:31], off offset:192
	s_nop 0
	global_load_dwordx4 v[36:39], v[48:49], off
	global_load_dwordx4 v[40:43], v[48:49], off offset:64
	global_load_dwordx4 v[44:47], v[48:49], off offset:128
	s_nop 0
	global_load_dwordx4 v[48:51], v[48:49], off offset:192
	s_nop 0
	global_load_dwordx4 v[52:55], v[64:65], off
	global_load_dwordx4 v[56:59], v[64:65], off offset:64
	global_load_dwordx4 v[60:63], v[64:65], off offset:128
	s_nop 0
	global_load_dwordx4 v[64:67], v[64:65], off offset:192
	v_add_u32_e32 v68, s2, v169
	global_load_dword v34, v34, s[78:79]
	v_ashrrev_i32_e32 v69, 31, v68
	s_mov_b32 s10, 0
	v_lshlrev_b64 v[70:71], 6, v[68:69]
	s_mov_b32 s11, 1
	s_mov_b32 s9, s10
	v_lshl_add_u64 v[70:71], s[80:81], 0, v[70:71]
	v_lshl_add_u64 v[70:71], v[70:71], 0, s[8:9]
	global_load_dword v86, v[70:71], off
	v_and_b32_e32 v70, 64, v203
	v_add_u32_e32 v71, -1, v203
	v_cmp_lt_i32_e32 vcc, v71, v70
	v_lshlrev_b64 v[68:69], 11, v[68:69]
	v_lshl_add_u64 v[68:69], s[76:77], 0, v[68:69]
	v_cndmask_b32_e32 v71, v71, v203, vcc
	v_lshlrev_b32_e32 v71, 2, v71
	s_lshl_b32 s8, s0, 7
	v_lshl_add_u64 v[84:85], v[68:69], 0, s[8:9]
	s_ashr_i32 s3, s2, 31
	v_mov_b32_e32 v155, v132
	v_mov_b32_e32 v157, v225
	v_mov_b32_e32 v159, v224
	v_mov_b32_e32 v161, v223
	v_mov_b32_e32 v235, v222
	s_waitcnt vmcnt(0)
	v_mul_f32_e32 v34, 0x3fb8aa3b, v34
	v_exp_f32_e32 v72, v34
	s_nop 0
	v_mul_f32_e64 v34, v86, -v72
	s_nop 1
	v_add_f32_dpp v34, v34, v34 row_shr:1 row_mask:0xf bank_mask:0xf
	v_add_u32_e32 v71, -2, v203
	v_cmp_lt_i32_e32 vcc, v71, v70
	s_nop 1
	v_cndmask_b32_e32 v71, v71, v203, vcc
	v_lshlrev_b32_e32 v71, 2, v71
	s_nop 1
	v_add_f32_dpp v34, v34, v34 row_shr:2 row_mask:0xf bank_mask:0xf
	v_add_u32_e32 v71, -4, v203
	v_cmp_lt_i32_e32 vcc, v71, v70
	s_nop 1
	v_cndmask_b32_e32 v71, v71, v203, vcc
	v_lshlrev_b32_e32 v71, 2, v71
	s_nop 1
	v_add_f32_dpp v34, v34, v34 row_shr:4 row_mask:0xf bank_mask:0xf
	v_add_u32_e32 v71, -8, v203
	v_cmp_lt_i32_e32 vcc, v71, v70
	s_nop 1
	v_cndmask_b32_e32 v71, v71, v203, vcc
	v_lshlrev_b32_e32 v71, 2, v71
	s_nop 1
	v_add_f32_dpp v34, v34, v34 row_shr:8 row_mask:0xf bank_mask:0xf
	v_add_u32_e32 v71, -16, v203
	v_cmp_lt_i32_e32 vcc, v71, v70
	s_nop 1
	v_cndmask_b32_e32 v71, v71, v203, vcc
	v_lshlrev_b32_e32 v71, 2, v71
	s_nop 1
	v_add_f32_dpp v34, v34, v34 row_bcast:15 row_mask:0xa bank_mask:0xf
	v_subrev_u32_e32 v71, 32, v203
	v_cmp_lt_i32_e32 vcc, v71, v70
	s_nop 1
	v_cndmask_b32_e32 v70, v71, v203, vcc
	v_lshlrev_b32_e32 v70, 2, v70
	s_nop 1
	v_add_f32_dpp v34, v34, v34 row_bcast:31 row_mask:0xc bank_mask:0xf
	v_mov_b32_e32 v70, v34
	v_fma_f32 v71, v86, v72, v70
	v_lshl_or_b32 v34, v203, 2, v251
	ds_write2st64_b32 v182, v70, v71 offset1:1
	ds_bpermute_b32 v34, v34, v70
	global_load_dwordx4 v[68:71], v[84:85], off offset:48
	global_load_dwordx4 v[72:75], v[84:85], off offset:32
	global_load_dwordx4 v[76:79], v[84:85], off offset:16
	global_load_dwordx4 v[80:83], v[84:85], off
	s_waitcnt vmcnt(0)
	v_lshlrev_b32_e32 v87, 16, v80
	v_and_b32_e32 v80, 0xffff0000, v80
	v_mul_f32_e32 v80, v86, v80
	v_lshlrev_b32_e32 v88, 16, v81
	v_cvt_pk_bf16_f32 v80, v80, s0
	ds_write_b16 v183, v80 offset:44176
	v_mul_f32_e32 v80, v86, v88
	v_and_b32_e32 v81, 0xffff0000, v81
	v_cvt_pk_bf16_f32 v80, v80, s0
	ds_write_b16 v183, v80 offset:44320
	v_mul_f32_e32 v80, v86, v81
	v_cvt_pk_bf16_f32 v80, v80, s0
	ds_write_b16 v183, v80 offset:44464
	v_lshlrev_b32_e32 v80, 16, v82
	v_mul_f32_e32 v80, v86, v80
	v_and_b32_e32 v81, 0xffff0000, v82
	v_cvt_pk_bf16_f32 v80, v80, s0
	ds_write_b16 v183, v80 offset:44608
	v_mul_f32_e32 v80, v86, v81
	v_lshlrev_b32_e32 v82, 16, v83
	v_cvt_pk_bf16_f32 v80, v80, s0
	ds_write_b16 v183, v80 offset:44752
	v_mul_f32_e32 v80, v86, v82
	v_and_b32_e32 v83, 0xffff0000, v83
	v_cvt_pk_bf16_f32 v80, v80, s0
	ds_write_b16 v183, v80 offset:44896
	v_mul_f32_e32 v80, v86, v83
	v_cvt_pk_bf16_f32 v80, v80, s0
	ds_write_b16 v183, v80 offset:45040
	v_lshlrev_b32_e32 v80, 16, v76
	v_and_b32_e32 v76, 0xffff0000, v76
	v_mul_f32_e32 v76, v86, v76
	v_lshlrev_b32_e32 v81, 16, v77
	v_cvt_pk_bf16_f32 v76, v76, s0
	ds_write_b16 v183, v76 offset:45328
	v_mul_f32_e32 v76, v86, v81
	v_and_b32_e32 v77, 0xffff0000, v77
	v_cvt_pk_bf16_f32 v76, v76, s0
	ds_write_b16 v183, v76 offset:45472
	v_mul_f32_e32 v76, v86, v77
	v_cvt_pk_bf16_f32 v76, v76, s0
	ds_write_b16 v183, v76 offset:45616
	v_lshlrev_b32_e32 v76, 16, v78
	v_mul_f32_e32 v76, v86, v76
	v_and_b32_e32 v77, 0xffff0000, v78
	v_cvt_pk_bf16_f32 v76, v76, s0
	ds_write_b16 v183, v76 offset:45760
	v_mul_f32_e32 v76, v86, v77
	v_lshlrev_b32_e32 v78, 16, v79
	v_cvt_pk_bf16_f32 v76, v76, s0
	ds_write_b16 v183, v76 offset:45904
	v_mul_f32_e32 v76, v86, v78
	v_and_b32_e32 v79, 0xffff0000, v79
	v_cvt_pk_bf16_f32 v76, v76, s0
	ds_write_b16 v183, v76 offset:46048
	v_mul_f32_e32 v76, v86, v79
	v_cvt_pk_bf16_f32 v76, v76, s0
	ds_write_b16 v183, v76 offset:46192
	v_lshlrev_b32_e32 v76, 16, v72
	v_and_b32_e32 v72, 0xffff0000, v72
	v_mul_f32_e32 v72, v86, v72
	v_lshlrev_b32_e32 v77, 16, v73
	v_cvt_pk_bf16_f32 v72, v72, s0
	ds_write_b16 v183, v72 offset:46480
	v_mul_f32_e32 v72, v86, v77
	v_and_b32_e32 v73, 0xffff0000, v73
	v_cvt_pk_bf16_f32 v72, v72, s0
	ds_write_b16 v183, v72 offset:46624
	v_mul_f32_e32 v72, v86, v73
	v_cvt_pk_bf16_f32 v72, v72, s0
	ds_write_b16 v183, v72 offset:46768
	v_lshlrev_b32_e32 v72, 16, v74
	v_mul_f32_e32 v72, v86, v72
	v_and_b32_e32 v73, 0xffff0000, v74
	v_cvt_pk_bf16_f32 v72, v72, s0
	ds_write_b16 v183, v72 offset:46912
	v_mul_f32_e32 v72, v86, v73
	v_lshlrev_b32_e32 v74, 16, v75
	v_cvt_pk_bf16_f32 v72, v72, s0
	ds_write_b16 v183, v72 offset:47056
	v_mul_f32_e32 v72, v86, v74
	v_and_b32_e32 v75, 0xffff0000, v75
	v_cvt_pk_bf16_f32 v72, v72, s0
	ds_write_b16 v183, v72 offset:47200
	v_mul_f32_e32 v72, v86, v75
	v_cvt_pk_bf16_f32 v72, v72, s0
	ds_write_b16 v183, v72 offset:47344
	v_lshlrev_b32_e32 v72, 16, v68
	v_and_b32_e32 v68, 0xffff0000, v68
	v_mul_f32_e32 v68, v86, v68
	v_lshlrev_b32_e32 v73, 16, v69
	v_cvt_pk_bf16_f32 v68, v68, s0
	ds_write_b16 v183, v68 offset:47632
	v_mul_f32_e32 v68, v86, v73
	v_and_b32_e32 v69, 0xffff0000, v69
	v_cvt_pk_bf16_f32 v68, v68, s0
	ds_write_b16 v183, v68 offset:47776
	v_mul_f32_e32 v68, v86, v69
	v_cvt_pk_bf16_f32 v68, v68, s0
	ds_write_b16 v183, v68 offset:47920
	v_lshlrev_b32_e32 v68, 16, v70
	v_mul_f32_e32 v68, v86, v68
	v_and_b32_e32 v69, 0xffff0000, v70
	v_cvt_pk_bf16_f32 v68, v68, s0
	ds_write_b16 v183, v68 offset:48064
	v_mul_f32_e32 v68, v86, v69
	v_lshlrev_b32_e32 v70, 16, v71
	v_cvt_pk_bf16_f32 v68, v68, s0
	ds_write_b16 v183, v68 offset:48208
	v_mul_f32_e32 v68, v86, v70
	v_and_b32_e32 v71, 0xffff0000, v71
	v_cvt_pk_bf16_f32 v68, v68, s0
	v_mul_f32_e32 v87, v86, v87
	v_mul_f32_e32 v80, v86, v80
	v_mul_f32_e32 v76, v86, v76
	v_mul_f32_e32 v72, v86, v72
	ds_write_b16 v183, v68 offset:48352
	v_mul_f32_e32 v68, v86, v71
	v_cvt_pk_bf16_f32 v87, v87, s0
	v_cvt_pk_bf16_f32 v80, v80, s0
	v_cvt_pk_bf16_f32 v76, v76, s0
	v_cvt_pk_bf16_f32 v72, v72, s0
	v_cvt_pk_bf16_f32 v68, v68, s0
	ds_write_b16 v183, v87 offset:44032
	ds_write_b16 v183, v80 offset:45184
	ds_write_b16 v183, v76 offset:46336
	ds_write_b16 v183, v72 offset:47488
	ds_write_b16 v183, v68 offset:48496
	global_load_dwordx4 v[68:71], v[84:85], off offset:112
	global_load_dwordx4 v[72:75], v[84:85], off offset:96
	global_load_dwordx4 v[76:79], v[84:85], off offset:80
	global_load_dwordx4 v[80:83], v[84:85], off offset:64
	s_waitcnt vmcnt(0)
	v_lshlrev_b32_e32 v84, 16, v80
	v_and_b32_e32 v80, 0xffff0000, v80
	v_mul_f32_e32 v80, v86, v80
	v_lshlrev_b32_e32 v85, 16, v81
	v_cvt_pk_bf16_f32 v80, v80, s0
	ds_write_b16 v183, v80 offset:48784
	v_mul_f32_e32 v80, v86, v85
	v_and_b32_e32 v81, 0xffff0000, v81
	v_cvt_pk_bf16_f32 v80, v80, s0
	ds_write_b16 v183, v80 offset:48928
	v_mul_f32_e32 v80, v86, v81
	v_cvt_pk_bf16_f32 v80, v80, s0
	ds_write_b16 v183, v80 offset:49072
	v_lshlrev_b32_e32 v80, 16, v82
	v_mul_f32_e32 v80, v86, v80
	v_and_b32_e32 v81, 0xffff0000, v82
	v_cvt_pk_bf16_f32 v80, v80, s0
	ds_write_b16 v183, v80 offset:49216
	v_mul_f32_e32 v80, v86, v81
	v_lshlrev_b32_e32 v82, 16, v83
	v_cvt_pk_bf16_f32 v80, v80, s0
	ds_write_b16 v183, v80 offset:49360
	v_mul_f32_e32 v80, v86, v82
	v_and_b32_e32 v83, 0xffff0000, v83
	v_cvt_pk_bf16_f32 v80, v80, s0
	ds_write_b16 v183, v80 offset:49504
	v_mul_f32_e32 v80, v86, v83
	v_cvt_pk_bf16_f32 v80, v80, s0
	ds_write_b16 v183, v80 offset:49648
	v_lshlrev_b32_e32 v80, 16, v76
	v_and_b32_e32 v76, 0xffff0000, v76
	v_mul_f32_e32 v76, v86, v76
	v_lshlrev_b32_e32 v81, 16, v77
	v_cvt_pk_bf16_f32 v76, v76, s0
	ds_write_b16 v183, v76 offset:49936
	v_mul_f32_e32 v76, v86, v81
	v_and_b32_e32 v77, 0xffff0000, v77
	v_cvt_pk_bf16_f32 v76, v76, s0
	ds_write_b16 v183, v76 offset:50080
	v_mul_f32_e32 v76, v86, v77
	v_cvt_pk_bf16_f32 v76, v76, s0
	ds_write_b16 v183, v76 offset:50224
	v_lshlrev_b32_e32 v76, 16, v78
	v_mul_f32_e32 v76, v86, v76
	v_and_b32_e32 v77, 0xffff0000, v78
	v_cvt_pk_bf16_f32 v76, v76, s0
	ds_write_b16 v183, v76 offset:50368
	v_mul_f32_e32 v76, v86, v77
	v_lshlrev_b32_e32 v78, 16, v79
	v_cvt_pk_bf16_f32 v76, v76, s0
	ds_write_b16 v183, v76 offset:50512
	v_mul_f32_e32 v76, v86, v78
	v_and_b32_e32 v79, 0xffff0000, v79
	v_cvt_pk_bf16_f32 v76, v76, s0
	ds_write_b16 v183, v76 offset:50656
	v_mul_f32_e32 v76, v86, v79
	v_cvt_pk_bf16_f32 v76, v76, s0
	ds_write_b16 v183, v76 offset:50800
	v_lshlrev_b32_e32 v76, 16, v72
	v_and_b32_e32 v72, 0xffff0000, v72
	v_mul_f32_e32 v72, v86, v72
	v_lshlrev_b32_e32 v77, 16, v73
	v_cvt_pk_bf16_f32 v72, v72, s0
	ds_write_b16 v183, v72 offset:51088
	v_mul_f32_e32 v72, v86, v77
	v_and_b32_e32 v73, 0xffff0000, v73
	v_cvt_pk_bf16_f32 v72, v72, s0
	ds_write_b16 v183, v72 offset:51232
	v_mul_f32_e32 v72, v86, v73
	v_cvt_pk_bf16_f32 v72, v72, s0
	ds_write_b16 v183, v72 offset:51376
	v_lshlrev_b32_e32 v72, 16, v74
	v_mul_f32_e32 v72, v86, v72
	v_and_b32_e32 v73, 0xffff0000, v74
	v_cvt_pk_bf16_f32 v72, v72, s0
	ds_write_b16 v183, v72 offset:51520
	v_mul_f32_e32 v72, v86, v73
	v_lshlrev_b32_e32 v74, 16, v75
	v_cvt_pk_bf16_f32 v72, v72, s0
	ds_write_b16 v183, v72 offset:51664
	v_mul_f32_e32 v72, v86, v74
	v_and_b32_e32 v75, 0xffff0000, v75
	v_cvt_pk_bf16_f32 v72, v72, s0
	ds_write_b16 v183, v72 offset:51808
	v_mul_f32_e32 v72, v86, v75
	v_cvt_pk_bf16_f32 v72, v72, s0
	ds_write_b16 v183, v72 offset:51952
	v_lshlrev_b32_e32 v72, 16, v68
	v_and_b32_e32 v68, 0xffff0000, v68
	v_mul_f32_e32 v68, v86, v68
	v_lshlrev_b32_e32 v73, 16, v69
	v_cvt_pk_bf16_f32 v68, v68, s0
	ds_write_b16 v183, v68 offset:52240
	v_mul_f32_e32 v68, v86, v73
	v_and_b32_e32 v69, 0xffff0000, v69
	v_cvt_pk_bf16_f32 v68, v68, s0
	ds_write_b16 v183, v68 offset:52384
	v_mul_f32_e32 v68, v86, v69
	v_cvt_pk_bf16_f32 v68, v68, s0
	ds_write_b16 v183, v68 offset:52528
	v_lshlrev_b32_e32 v68, 16, v70
	v_mul_f32_e32 v68, v86, v68
	v_and_b32_e32 v69, 0xffff0000, v70
	v_cvt_pk_bf16_f32 v68, v68, s0
	ds_write_b16 v183, v68 offset:52672
	v_mul_f32_e32 v68, v86, v69
	v_lshlrev_b32_e32 v70, 16, v71
	v_cvt_pk_bf16_f32 v68, v68, s0
	ds_write_b16 v183, v68 offset:52816
	v_mul_f32_e32 v68, v86, v70
	v_and_b32_e32 v71, 0xffff0000, v71
	v_cvt_pk_bf16_f32 v68, v68, s0
	v_mul_f32_e32 v84, v86, v84
	v_mul_f32_e32 v80, v86, v80
	v_mul_f32_e32 v76, v86, v76
	v_mul_f32_e32 v72, v86, v72
	ds_write_b16 v183, v68 offset:52960
	v_mul_f32_e32 v68, v86, v71
	v_cvt_pk_bf16_f32 v84, v84, s0
	v_cvt_pk_bf16_f32 v80, v80, s0
	v_cvt_pk_bf16_f32 v76, v76, s0
	v_cvt_pk_bf16_f32 v72, v72, s0
	v_cvt_pk_bf16_f32 v68, v68, s0
	ds_write_b16 v183, v84 offset:48640
	ds_write_b16 v183, v80 offset:49792
	ds_write_b16 v183, v76 offset:50944
	ds_write_b16 v183, v72 offset:52096
	ds_write_b16 v183, v68 offset:53104
	s_waitcnt lgkmcnt(0)
	s_barrier
	ds_read_b128 v[68:71], v184
	ds_read_b128 v[72:75], v232 offset:17408
	s_waitcnt lgkmcnt(0)
	v_mfma_f32_16x16x32_bf16 v[68:71], v[68:71], v[72:75], 0
	ds_read_b128 v[72:75], v184 offset:64
	ds_read_b128 v[76:79], v232 offset:17472
	s_waitcnt lgkmcnt(0)
	v_mfma_f32_16x16x32_bf16 v[68:71], v[72:75], v[76:79], v[68:71]
	ds_read_b128 v[72:75], v184 offset:128
	ds_read_b128 v[76:79], v232 offset:17536
	s_waitcnt lgkmcnt(0)
	v_mfma_f32_16x16x32_bf16 v[68:71], v[72:75], v[76:79], v[68:71]
	ds_read_b128 v[72:75], v184 offset:192
	ds_read_b128 v[76:79], v232 offset:17600
	s_waitcnt lgkmcnt(0)
	v_mfma_f32_16x16x32_bf16 v[68:71], v[72:75], v[76:79], v[68:71]
	v_add_u32_e32 v72, v185, v186
	s_nop 6
	v_cvt_pk_bf16_f32 v68, v68, s0
	ds_write_b16 v72, v68 offset:34816
	v_cvt_pk_bf16_f32 v68, v69, s0
	ds_write_b16 v72, v68 offset:34960
	v_cvt_pk_bf16_f32 v68, v70, s0
	ds_write_b16 v72, v68 offset:35104
	v_cvt_pk_bf16_f32 v68, v71, s0
	ds_write_b16 v72, v68 offset:35248
	ds_read_b128 v[68:71], v184
	ds_read_b128 v[72:75], v232 offset:21760
	s_waitcnt lgkmcnt(0)
	v_mfma_f32_16x16x32_bf16 v[68:71], v[68:71], v[72:75], 0
	ds_read_b128 v[72:75], v184 offset:64
	ds_read_b128 v[76:79], v232 offset:21824
	s_waitcnt lgkmcnt(0)
	v_mfma_f32_16x16x32_bf16 v[68:71], v[72:75], v[76:79], v[68:71]
	ds_read_b128 v[72:75], v184 offset:128
	ds_read_b128 v[76:79], v232 offset:21888
	s_waitcnt lgkmcnt(0)
	v_mfma_f32_16x16x32_bf16 v[68:71], v[72:75], v[76:79], v[68:71]
	ds_read_b128 v[72:75], v184 offset:192
	ds_read_b128 v[76:79], v232 offset:21952
	s_waitcnt lgkmcnt(0)
	v_mfma_f32_16x16x32_bf16 v[68:71], v[72:75], v[76:79], v[68:71]
	s_nop 7
	v_cvt_pk_bf16_f32 v68, v68, s0
	ds_write_b16 v233, v68 offset:34816
	v_cvt_pk_bf16_f32 v68, v69, s0
	ds_write_b16 v233, v68 offset:34960
	v_cvt_pk_bf16_f32 v68, v70, s0
	ds_write_b16 v233, v68 offset:35104
	v_cvt_pk_bf16_f32 v68, v71, s0
	ds_write_b16 v233, v68 offset:35248
	s_waitcnt lgkmcnt(0)
	s_barrier
	ds_read_b128 v[68:71], v234 offset:44032
	ds_read_b128 v[72:75], v234 offset:46336
	ds_read_b128 v[76:79], v234 offset:48640
	ds_read_b128 v[80:83], v234 offset:50944
	ds_read_b128 v[84:87], v234 offset:44096
	ds_read_b128 v[88:91], v234 offset:46400
	ds_read_b128 v[92:95], v234 offset:48704
	ds_read_b128 v[96:99], v234 offset:51008
	s_lshl_b64 s[0:1], s[2:3], 10
	s_or_b32 s0, s0, s8
	v_lshl_add_u64 v[162:163], v[152:153], 0, s[0:1]
	s_mov_b64 s[2:3], 0
	s_branch .LBB0_1028
